# attention softmax bodies (FoX, SWA, cross): SLP-packed v_pk_add_f32 row-sum / max-subtract ops rewritten as scalar v_add/v_sub, dead halves dropped
# speedup vs baseline: 1.0016x; 1.0016x over previous
; __global__ void __launch_bounds__(NTHREADS, 2) mk_fwd(Args args) {
;     ...
;               float woff = 0.f;
;               for (int w = 0; w < F.wave; ++w) woff += wtot[w];
;               const float base = woff + sc - tot;
; #pragma unroll
;               for (int j = 0; j < 8; ++j) cl[tidv * 8 + j] = base + pre[j];
;               __syncthreads(); }
.LBB0_428:
	v_cmp_gt_u32_e32 vcc, 32, v1
	s_mov_b32 s46, s80
	s_nop 0
	v_cndmask_b32_e32 v1, v11, v2, vcc
	v_add_f32_e32 v1, v1, v14
	v_sub_f32_e32 v2, v1, v7
	v_lshl_add_u32 v1, v10, 2, 0
	v_add_u32_e32 v1, 0x11000, v1
	v_add_f32_e32 v11, v2, v5
	v_add_f32_e32 v10, v2, v4
	v_add_f32_e32 v13, v2, v13
	v_add_f32_e32 v12, v2, v12
	v_add_f32_e32 v5, v2, v9
	v_add_f32_e32 v4, v2, v8
	v_add_f32_e32 v7, v2, v7
	v_add_f32_e32 v6, v2, v6
	ds_write_b128 v1, v[10:13]
	ds_write_b128 v1, v[4:7] offset:16
	s_waitcnt lgkmcnt(0)
	s_barrier

; #define LAS __attribute__((address_space(3)))
; __device__ __forceinline__ unsigned cvtpk(float lo, float hi) { typedef __bf16 bf16x2_t __attribute__((ext_vector_type(2))); f32x2 v = {lo, hi}; bf16x2_t b = __builtin_convertvector(v, bf16x2_t); return __builtin_bit_cast(unsigned, b); }
; __device__ __forceinline__ s16x4 vtr(const LAS unsigned char* p) { return __builtin_bit_cast(s16x4, __builtin_amdgcn_ds_read_tr16_b64_v4i16((LAS v4i16_t*)p)); }
; template <int D, bool MASK, bool BIAS, bool SINK, bool REV, bool O8, class BG>
; __device__ __forceinline__ void attn_unit(const Prm& P, LAS unsigned char* lds, BG& bg) {
;     ...
;             float sacc = 0.f;
; #pragma unroll
;             for (int r = 0; r < 16; ++r) { p0[r] = __builtin_amdgcn_exp2f(p0[r]); p1[r] = __builtin_amdgcn_exp2f(p1[r]); sacc += p0[r] + p1[r]; }
;             l_reg += sacc;
;             u32x4 pw[4];
; #pragma unroll
;             for (int q = 0; q < 4; ++q) { pw[0][q] = cvtpk(p0[2 * q], p0[2 * q + 1]); pw[1][q] = cvtpk(p0[8 + 2 * q], p0[9 + 2 * q]); pw[2][q] = cvtpk(p1[2 * q], p1[2 * q + 1]); pw[3][q] = cvtpk(p1[8 + 2 * q], p1[9 + 2 * q]); }
;             const LAS unsigned char* vs = lds + VOFF + s * KSLOT + ((lane >> 4) & 1) * 32 + (lane & 3) * 8 + (4 * hi + ((lane & 15) >> 2)) * 64;
; #pragma unroll
;             for (int d = 0; d < NDB; ++d)
; #pragma unroll
;                 for (int k4 = 0; k4 < 4; ++k4) {
;                     const s16x4 vlo = vtr(vs + d * 4096 + k4 * 1024), vhi = vtr(vs + d * 4096 + k4 * 1024 + 512);
;                     const bf16x8 vf = (bf16x8){vlo[0], vlo[1], vlo[2], vlo[3], vhi[0], vhi[1], vhi[2], vhi[3]};
;                     o[d] = __builtin_amdgcn_mfma_f32_32x32x16_bf16(__builtin_bit_cast(bf16x8, pw[k4]), vf, o[d], 0, 0, 0);
;                 }
.LBB0_477:
	v_exp_f32_e32 v78, v2
	v_exp_f32_e32 v79, v64
	v_exp_f32_e32 v2, v1
	v_exp_f32_e32 v66, v65
	v_exp_f32_e32 v1, v58
	v_add_f32_e32 v67, v79, v78
	v_exp_f32_e32 v68, v63
	v_add_f32_e32 v65, v67, v3
	v_add_f32_e32 v64, v66, v2
	v_exp_f32_e32 v67, v62
	v_add_f32_e32 v65, v64, v65
	v_exp_f32_e32 v64, v59
	v_exp_f32_e32 v62, v61
	v_add_f32_e32 v69, v67, v1
	v_exp_f32_e32 v42, v42
	v_add_f32_e32 v59, v69, v65
	v_add_f32_e32 v58, v68, v64
	v_exp_f32_e32 v65, v54
	v_add_f32_e32 v59, v58, v59
	v_exp_f32_e32 v69, v60
	v_exp_f32_e32 v58, v55
	v_exp_f32_e32 v60, v57
	v_exp_f32_e32 v72, v45
	v_add_f32_e32 v63, v69, v65
	v_add_f32_e32 v55, v63, v59
	v_add_f32_e32 v54, v62, v58
	v_exp_f32_e32 v59, v50
	v_add_f32_e32 v55, v54, v55
	v_exp_f32_e32 v63, v56
	v_exp_f32_e32 v54, v51
	v_exp_f32_e32 v56, v53
	v_exp_f32_e32 v76, v43
	v_add_f32_e32 v61, v63, v59
	v_add_f32_e32 v51, v61, v55
	v_add_f32_e32 v50, v60, v54
	v_exp_f32_e32 v55, v46
	v_add_f32_e32 v51, v50, v51
	v_exp_f32_e32 v61, v52
	v_exp_f32_e32 v50, v47
	v_exp_f32_e32 v52, v49
	v_cvt_pk_bf16_f32 v43, v59, v54
	v_add_f32_e32 v57, v61, v55
	v_add_f32_e32 v47, v57, v51
	v_add_f32_e32 v46, v56, v50
	v_exp_f32_e32 v51, v48
	v_add_f32_e32 v47, v46, v47
	v_exp_f32_e32 v46, v41
	v_exp_f32_e32 v57, v40
	v_add_f32_e32 v53, v51, v42
	v_cvt_pk_bf16_f32 v41, v1, v64
	v_add_f32_e32 v49, v53, v47
	v_add_f32_e32 v48, v52, v46
	v_exp_f32_e32 v47, v38
	v_add_f32_e32 v71, v48, v49
	v_exp_f32_e32 v53, v44
	v_exp_f32_e32 v70, v39
	v_add_u32_e32 v1, s14, v194
	v_cvt_pk_bf16_f32 v40, v78, v2
	v_add_f32_e32 v73, v53, v47
	v_add_f32_e32 v39, v73, v71
	v_add_f32_e32 v38, v72, v70
	v_cvt_pk_bf16_f32 v44, v55, v50
	v_add_f32_e32 v75, v38, v39
	v_exp_f32_e32 v39, v36
	v_exp_f32_e32 v74, v37
	v_cvt_pk_bf16_f32 v45, v42, v46
	v_cvt_pk_bf16_f32 v42, v65, v58
	v_add_f32_e32 v77, v57, v39
	v_add_f32_e32 v37, v77, v75
	v_add_f32_e32 v36, v76, v74
	v_cvt_pk_bf16_f32 v38, v53, v72
	v_add_f32_e32 v71, v36, v37
	v_cvt_pk_bf16_f32 v37, v51, v52
	s_nop 0
	ds_read_b64_tr_b16 v[52:53], v1 offset:32768
	ds_read_b64_tr_b16 v[54:55], v1 offset:33280
	ds_read_b64_tr_b16 v[240:241], v1 offset:33792
	ds_read_b64_tr_b16 v[242:243], v1 offset:34304
	ds_read_b64_tr_b16 v[244:245], v1 offset:34816
	ds_read_b64_tr_b16 v[246:247], v1 offset:35328
	ds_read_b64_tr_b16 v[248:249], v1 offset:35840
	ds_read_b64_tr_b16 v[250:251], v1 offset:36352
	v_cvt_pk_bf16_f32 v46, v47, v70
	v_cvt_pk_bf16_f32 v47, v39, v74
	s_waitcnt lgkmcnt(6)
	v_mfma_f32_32x32x16_bf16 v[4:19], v[40:43], v[52:55], v[4:19]
	ds_read_b64_tr_b16 v[52:53], v1 offset:36864
	ds_read_b64_tr_b16 v[54:55], v1 offset:37376
	v_cvt_pk_bf16_f32 v48, v79, v66
	v_cvt_pk_bf16_f32 v49, v67, v68
	v_cvt_pk_bf16_f32 v50, v69, v62
	v_cvt_pk_bf16_f32 v51, v63, v60
	s_waitcnt lgkmcnt(6)
	v_mfma_f32_32x32x16_bf16 v[4:19], v[44:47], v[240:243], v[4:19]
	ds_read_b64_tr_b16 v[240:241], v1 offset:37888
	ds_read_b64_tr_b16 v[242:243], v1 offset:38400
	v_cvt_pk_bf16_f32 v36, v61, v56
	v_cvt_pk_bf16_f32 v39, v57, v76
	v_add_f32_e32 v225, v225, v71
	s_mov_b64 s[92:93], 0
	s_waitcnt lgkmcnt(6)
	v_mfma_f32_32x32x16_bf16 v[4:19], v[48:51], v[244:247], v[4:19]
	ds_read_b64_tr_b16 v[244:245], v1 offset:38912
	ds_read_b64_tr_b16 v[246:247], v1 offset:39424
	s_waitcnt lgkmcnt(6)
	v_mfma_f32_32x32x16_bf16 v[4:19], v[36:39], v[248:251], v[4:19]
	ds_read_b64_tr_b16 v[248:249], v1 offset:39936
	ds_read_b64_tr_b16 v[250:251], v1 offset:40448
	s_waitcnt lgkmcnt(6)
	v_mfma_f32_32x32x16_bf16 v[20:35], v[40:43], v[52:55], v[20:35]
	s_waitcnt lgkmcnt(4)
	v_mfma_f32_32x32x16_bf16 v[20:35], v[44:47], v[240:243], v[20:35]
	s_waitcnt lgkmcnt(2)
	v_mfma_f32_32x32x16_bf16 v[20:35], v[48:51], v[244:247], v[20:35]
	s_waitcnt lgkmcnt(0)
	v_mfma_f32_32x32x16_bf16 v[20:35], v[36:39], v[248:251], v[20:35]

; template <int D, bool MASK, bool BIAS, bool SINK, bool REV, bool O8, class BG>
; __device__ __forceinline__ void attn_unit(const Prm& P, LAS unsigned char* lds, BG& bg) {
;     ...
;             float a = max3f(p0[0], p0[1], p1[0]), b = max3f(p0[2], p0[3], p1[1]); a = max3f(a, p1[2], p1[3]);
; #pragma unroll
;             for (int r = 4; r < 16; r += 4) { a = max3f(a, p0[r], p0[r + 1]); b = max3f(b, p0[r + 2], p0[r + 3]); a = max3f(a, p1[r], p1[r + 1]); b = max3f(b, p1[r + 2], p1[r + 3]); }
;             float rm = __builtin_fmaxf(a, b);
;             { auto rr = __builtin_amdgcn_permlane32_swap(__float_as_uint(rm), __float_as_uint(rm), false, false); rm = __builtin_fmaxf(__uint_as_float(rr[0]), __uint_as_float(rr[1])); }
;             if (first || __any(rm > THR)) {
;                 float dl = first ? rm : __builtin_fmaxf(rm, 0.f);
;                 if (!(dl > -1e30f)) dl = 0.f;
;                 mhat += dl;
; #pragma unroll
;                 for (int r = 0; r < 16; ++r) { p0[r] -= dl; p1[r] -= dl; }
;                 if (!first) {
;                     const float f = __builtin_amdgcn_exp2f(-dl); l_reg *= f;
;                     if (hi == 0) wsf[r32] = f;
;                     LDS_WAIT();
; #pragma unroll
;                     for (int g = 0; g < 4; ++g) { const f32x4 fv = *(const LAS f32x4*)(wsf + 8 * g + 4 * hi);
; #pragma unroll
;                         for (int d = 0; d < NDB; ++d)
; #pragma unroll
;                             for (int j = 0; j < 4; ++j) o[d][4 * g + j] *= fv[j]; }
;                 }
;                 first = false;
;             }
;             float sacc = 0.f;
; #pragma unroll
;             for (int r = 0; r < 16; ++r) { p0[r] = __builtin_amdgcn_exp2f(p0[r]); p1[r] = __builtin_amdgcn_exp2f(p1[r]); sacc += p0[r] + p1[r]; }
;             l_reg += sacc;
;             u32x4 pw[4];
; #pragma unroll
;             for (int q = 0; q < 4; ++q) { pw[0][q] = cvtpk(p0[2 * q], p0[2 * q + 1]); pw[1][q] = cvtpk(p0[8 + 2 * q], p0[9 + 2 * q]); pw[2][q] = cvtpk(p1[2 * q], p1[2 * q + 1]); pw[3][q] = cvtpk(p1[8 + 2 * q], p1[9 + 2 * q]); }
;             const LAS unsigned char* vs = lds + VOFF + s * KSLOT + ((lane >> 4) & 1) * 32 + (lane & 3) * 8 + (4 * hi + ((lane & 15) >> 2)) * 64;
; #pragma unroll
;             for (int d = 0; d < NDB; ++d)
; #pragma unroll
;                 for (int k4 = 0; k4 < 4; ++k4) {
.LBB0_606:
	v_max_f32_e32 v82, v51, v51
	v_max_f32_e32 v91, v50, v50
	v_max_f32_e32 v82, v91, v82
	v_max3_f32 v91, v52, v53, v35
	v_max3_f32 v82, v82, v34, v36
	v_max3_f32 v82, v82, v37, v54
	v_max3_f32 v91, v91, v56, v57
	v_max3_f32 v82, v82, v55, v38
	v_max3_f32 v91, v91, v40, v41
	v_max3_f32 v82, v82, v39, v58
	v_max3_f32 v91, v91, v60, v61
	v_max3_f32 v82, v82, v59, v42
	v_max3_f32 v91, v91, v44, v45
	v_max3_f32 v82, v82, v43, v62
	v_max3_f32 v91, v91, v64, v65
	v_max3_f32 v82, v82, v63, v46
	v_max3_f32 v91, v91, v48, v49
	v_max3_f32 v82, v82, v47, v91
	v_mov_b32_e32 v91, v82
	s_nop 1
	v_permlane32_swap_b32_e32 v82, v91
	v_max_f32_e32 v91, v91, v91
	v_max_f32_e32 v82, v82, v82
	v_max_f32_e32 v82, v82, v91
	s_mov_b32 s6, 0x41000000
	v_cmp_lt_f32_e32 vcc, s6, v82
	s_cbranch_vccz .LBB0_610
	v_max_f32_e32 v82, v82, v82
	v_max_f32_e32 v82, 0, v82
	v_exp_f32_e64 v91, -v82
	s_and_saveexec_b64 s[6:7], s[4:5]
	ds_write_b32 v189, v91
	s_or_b64 exec, exec, s[6:7]
	s_waitcnt lgkmcnt(0)
	ds_read_b128 v[192:195], v191
	ds_read_b128 v[196:199], v191 offset:32
	ds_read_b128 v[200:203], v191 offset:64
	ds_read_b128 v[204:207], v191 offset:96
	v_sub_f32_e32 v51, v51, v82
	v_sub_f32_e32 v50, v50, v82
	v_sub_f32_e32 v35, v35, v82
	v_sub_f32_e32 v34, v34, v82
	v_sub_f32_e32 v53, v53, v82
	v_sub_f32_e32 v52, v52, v82
	v_sub_f32_e32 v37, v37, v82
	v_sub_f32_e32 v36, v36, v82
	v_sub_f32_e32 v55, v55, v82
	v_sub_f32_e32 v54, v54, v82
	v_sub_f32_e32 v39, v39, v82
	v_sub_f32_e32 v38, v38, v82
	v_sub_f32_e32 v57, v57, v82
	v_sub_f32_e32 v56, v56, v82
	v_sub_f32_e32 v41, v41, v82
	v_sub_f32_e32 v40, v40, v82
	v_sub_f32_e32 v59, v59, v82
	v_sub_f32_e32 v58, v58, v82
	v_sub_f32_e32 v43, v43, v82
	v_sub_f32_e32 v42, v42, v82
	v_sub_f32_e32 v61, v61, v82
	v_sub_f32_e32 v60, v60, v82
	v_sub_f32_e32 v45, v45, v82
	v_sub_f32_e32 v44, v44, v82
	v_sub_f32_e32 v63, v63, v82
	v_sub_f32_e32 v62, v62, v82
	v_sub_f32_e32 v47, v47, v82
	v_sub_f32_e32 v46, v46, v82
	v_sub_f32_e32 v65, v65, v82
	v_sub_f32_e32 v64, v64, v82
	v_sub_f32_e32 v49, v49, v82
	v_sub_f32_e32 v48, v48, v82
	v_add_f32_e32 v188, v188, v82
	v_mul_f32_e32 v87, v87, v91
	s_waitcnt lgkmcnt(0)
	v_pk_mul_f32 v[32:33], v[32:33], v[206:207]
	v_pk_mul_f32 v[28:29], v[28:29], v[202:203]
	v_pk_mul_f32 v[24:25], v[24:25], v[198:199]
	v_pk_mul_f32 v[20:21], v[20:21], v[194:195]
	v_pk_mul_f32 v[16:17], v[16:17], v[206:207]
	v_pk_mul_f32 v[12:13], v[12:13], v[202:203]
	v_pk_mul_f32 v[8:9], v[8:9], v[198:199]
	v_pk_mul_f32 v[4:5], v[4:5], v[194:195]
	v_pk_mul_f32 v[30:31], v[30:31], v[204:205]
	v_pk_mul_f32 v[26:27], v[26:27], v[200:201]
	v_pk_mul_f32 v[22:23], v[22:23], v[196:197]
	v_pk_mul_f32 v[18:19], v[18:19], v[192:193]
	v_pk_mul_f32 v[14:15], v[14:15], v[204:205]
	v_pk_mul_f32 v[10:11], v[10:11], v[200:201]
	v_pk_mul_f32 v[6:7], v[6:7], v[196:197]
	v_pk_mul_f32 v[2:3], v[2:3], v[192:193]
.LBB0_610:
	v_exp_f32_e32 v91, v50
	v_exp_f32_e32 v200, v34
	v_exp_f32_e32 v82, v51
	v_exp_f32_e32 v192, v35
	v_exp_f32_e32 v201, v36
	v_add_f32_e32 v193, v200, v91
	v_exp_f32_e32 v194, v37
	v_add_f32_e32 v35, v193, v83
	v_add_f32_e32 v34, v192, v82
	v_exp_f32_e32 v193, v52
	v_add_f32_e32 v51, v34, v35
	v_exp_f32_e32 v50, v53
	v_exp_f32_e32 v202, v42
	v_add_f32_e32 v195, v201, v193
	v_add_f32_e32 v35, v195, v51
	v_add_f32_e32 v34, v194, v50
	s_nop 0
	v_add_f32_e32 v37, v34, v35
	v_exp_f32_e32 v51, v54
	v_exp_f32_e32 v195, v38
	v_exp_f32_e32 v36, v55
	v_exp_f32_e32 v54, v39
	v_add_f32_e32 v55, v195, v51
	v_add_f32_e32 v35, v55, v37
	v_add_f32_e32 v34, v54, v36
	s_nop 0
	v_add_f32_e32 v39, v34, v35
	v_exp_f32_e32 v37, v56
	v_exp_f32_e32 v55, v40
	v_exp_f32_e32 v38, v57
	v_exp_f32_e32 v56, v41
	v_cvt_pk_bf16_f32 v36, v51, v36
	v_add_f32_e32 v57, v55, v37
	v_cvt_pk_bf16_f32 v37, v37, v38
	v_add_f32_e32 v35, v57, v39
	v_add_f32_e32 v34, v56, v38
	v_exp_f32_e32 v57, v58
	v_add_f32_e32 v53, v34, v35
	v_exp_f32_e32 v52, v59
	v_exp_f32_e32 v58, v43
	v_add_f32_e32 v59, v202, v57
	v_exp_f32_e32 v43, v60
	v_exp_f32_e32 v60, v45
	v_add_f32_e32 v35, v59, v53
	v_add_f32_e32 v34, v58, v52
	v_exp_f32_e32 v59, v44
	v_add_f32_e32 v197, v34, v35
	v_exp_f32_e32 v196, v61
	v_cvt_pk_bf16_f32 v42, v57, v52
	v_add_f32_e32 v61, v59, v43
	v_add_f32_e32 v35, v61, v197
	v_add_f32_e32 v34, v60, v196
	s_nop 0
	v_add_f32_e32 v45, v34, v35
	v_exp_f32_e32 v61, v62
	v_exp_f32_e32 v197, v46
	v_exp_f32_e32 v44, v63
	v_exp_f32_e32 v62, v47
	v_cvt_pk_bf16_f32 v43, v43, v196
	v_add_f32_e32 v63, v197, v61
	v_cvt_pk_bf16_f32 v46, v202, v58
	v_add_f32_e32 v35, v63, v45
	v_add_f32_e32 v34, v62, v44
	v_exp_f32_e32 v63, v64
	v_add_f32_e32 v199, v34, v35
	v_cvt_pk_bf16_f32 v34, v91, v82
	v_add_u32_e32 v82, s14, v162
	v_cvt_pk_bf16_f32 v35, v193, v50
	s_nop 0
	ds_read_b64_tr_b16 v[38:39], v82 offset:32768
	ds_read_b64_tr_b16 v[40:41], v82 offset:33280
	v_exp_f32_e32 v198, v65
	s_waitcnt lgkmcnt(0)
	v_mfma_f32_32x32x16_bf16 v[2:17], v[34:37], v[38:41], v[2:17]
	ds_read_b64_tr_b16 v[50:51], v82 offset:33792
	ds_read_b64_tr_b16 v[52:53], v82 offset:34304
	v_cvt_pk_bf16_f32 v44, v61, v44
	v_cvt_pk_bf16_f32 v45, v63, v198
	v_cvt_pk_bf16_f32 v38, v200, v192
	v_cvt_pk_bf16_f32 v39, v201, v194
	v_cvt_pk_bf16_f32 v40, v195, v54
	v_cvt_pk_bf16_f32 v41, v55, v56
	s_waitcnt lgkmcnt(0)
	v_mfma_f32_32x32x16_bf16 v[2:17], v[42:45], v[50:53], v[2:17]
	ds_read_b64_tr_b16 v[50:51], v82 offset:34816
	ds_read_b64_tr_b16 v[52:53], v82 offset:35328
	v_exp_f32_e32 v61, v48
	v_exp_f32_e32 v64, v49
	ds_read_b64_tr_b16 v[54:55], v82 offset:35840
	ds_read_b64_tr_b16 v[56:57], v82 offset:36352
	v_cvt_pk_bf16_f32 v47, v59, v60
	v_cvt_pk_bf16_f32 v48, v197, v62
	v_cvt_pk_bf16_f32 v49, v61, v64
	s_waitcnt lgkmcnt(2)
	v_mfma_f32_32x32x16_bf16 v[2:17], v[38:41], v[50:53], v[2:17]
	v_add_f32_e32 v65, v61, v63
	s_waitcnt lgkmcnt(0)
	v_mfma_f32_32x32x16_bf16 v[2:17], v[46:49], v[54:57], v[2:17]
	ds_read_b64_tr_b16 v[50:51], v82 offset:36864
	ds_read_b64_tr_b16 v[52:53], v82 offset:37376
	ds_read_b64_tr_b16 v[54:55], v82 offset:37888
	ds_read_b64_tr_b16 v[56:57], v82 offset:38400
	s_waitcnt lgkmcnt(2)
	v_mfma_f32_32x32x16_bf16 v[18:33], v[34:37], v[50:53], v[18:33]
	s_waitcnt lgkmcnt(0)
	v_mfma_f32_32x32x16_bf16 v[18:33], v[42:45], v[54:57], v[18:33]
	ds_read_b64_tr_b16 v[34:35], v82 offset:38912
	ds_read_b64_tr_b16 v[36:37], v82 offset:39424
	ds_read_b64_tr_b16 v[42:43], v82 offset:39936
	ds_read_b64_tr_b16 v[44:45], v82 offset:40448
	s_waitcnt lgkmcnt(2)
	v_mfma_f32_32x32x16_bf16 v[18:33], v[38:41], v[34:37], v[18:33]
	v_add_f32_e64 v34, v64, v198
	v_add_f32_e64 v35, v65, v199
	v_add_f32_e32 v34, v34, v35
	v_add_f32_e32 v87, v87, v34
	s_waitcnt lgkmcnt(0)
	v_mfma_f32_32x32x16_bf16 v[18:33], v[46:49], v[42:45], v[18:33]

; #define LAS __attribute__((address_space(3)))
; __device__ __forceinline__ unsigned cvtpk(float lo, float hi) { typedef __bf16 bf16x2_t __attribute__((ext_vector_type(2))); f32x2 v = {lo, hi}; bf16x2_t b = __builtin_convertvector(v, bf16x2_t); return __builtin_bit_cast(unsigned, b); }
; __device__ __forceinline__ s16x4 vtr(const LAS unsigned char* p) { return __builtin_bit_cast(s16x4, __builtin_amdgcn_ds_read_tr16_b64_v4i16((LAS v4i16_t*)p)); }
; template <int D, bool MASK, bool BIAS, bool SINK, bool REV, bool O8, class BG>
; __device__ __forceinline__ void attn_unit(const Prm& P, LAS unsigned char* lds, BG& bg) {
;     ...
;             float sacc = 0.f;
; #pragma unroll
;             for (int r = 0; r < 16; ++r) { p0[r] = __builtin_amdgcn_exp2f(p0[r]); p1[r] = __builtin_amdgcn_exp2f(p1[r]); sacc += p0[r] + p1[r]; }
;             l_reg += sacc;
;             u32x4 pw[4];
; #pragma unroll
;             for (int q = 0; q < 4; ++q) { pw[0][q] = cvtpk(p0[2 * q], p0[2 * q + 1]); pw[1][q] = cvtpk(p0[8 + 2 * q], p0[9 + 2 * q]); pw[2][q] = cvtpk(p1[2 * q], p1[2 * q + 1]); pw[3][q] = cvtpk(p1[8 + 2 * q], p1[9 + 2 * q]); }
;             const LAS unsigned char* vs = lds + VOFF + s * KSLOT + ((lane >> 4) & 1) * 32 + (lane & 3) * 8 + (4 * hi + ((lane & 15) >> 2)) * 64;
; #pragma unroll
;             for (int d = 0; d < NDB; ++d)
; #pragma unroll
;                 for (int k4 = 0; k4 < 4; ++k4) {
;                     const s16x4 vlo = vtr(vs + d * 4096 + k4 * 1024), vhi = vtr(vs + d * 4096 + k4 * 1024 + 512);
;                     const bf16x8 vf = (bf16x8){vlo[0], vlo[1], vlo[2], vlo[3], vhi[0], vhi[1], vhi[2], vhi[3]};
;                     o[d] = __builtin_amdgcn_mfma_f32_32x32x16_bf16(__builtin_bit_cast(bf16x8, pw[k4]), vf, o[d], 0, 0, 0);
;                 }
.LBB0_940:
	v_exp_f32_e32 v2, v84
	v_exp_f32_e32 v135, v68
	v_exp_f32_e32 v151, v85
	v_exp_f32_e32 v156, v69
	v_exp_f32_e32 v86, v86
	v_exp_f32_e32 v157, v70
	v_exp_f32_e32 v87, v87
	v_exp_f32_e32 v158, v71
	v_add_f32_e32 v68, v135, v2
	v_exp_f32_e32 v159, v88
	v_exp_f32_e32 v160, v72
	v_add_f32_e32 v68, 0, v68
	v_add_f32_e32 v69, v156, v151
	v_exp_f32_e32 v70, v89
	v_exp_f32_e32 v88, v73
	v_add_f32_e32 v68, v69, v68
	v_add_f32_e32 v69, v157, v86
	v_add_f32_e32 v68, v69, v68
	v_add_f32_e32 v69, v158, v87
	v_add_f32_e32 v71, v69, v68
	v_add_f32_e32 v89, v160, v159
	v_add_f32_e32 v69, v89, v71
	v_add_f32_e32 v68, v88, v70
	v_exp_f32_e32 v71, v90
	v_add_f32_e32 v73, v68, v69
	v_exp_f32_e32 v89, v74
	v_exp_f32_e32 v72, v91
	v_exp_f32_e32 v90, v75
	v_exp_f32_e32 v161, v76
	v_add_f32_e32 v91, v89, v71
	v_cvt_pk_bf16_f32 v70, v159, v70
	v_add_f32_e32 v69, v91, v73
	v_add_f32_e32 v68, v90, v72
	v_exp_f32_e32 v91, v92
	v_add_f32_e32 v85, v68, v69
	v_exp_f32_e32 v84, v93
	v_exp_f32_e32 v92, v77
	v_add_f32_e32 v93, v161, v91
	v_exp_f32_e32 v77, v94
	v_exp_f32_e32 v94, v79
	v_add_f32_e32 v69, v93, v85
	v_add_f32_e32 v68, v92, v84
	v_exp_f32_e32 v93, v78
	v_add_f32_e32 v153, v68, v69
	v_exp_f32_e32 v152, v95
	v_cvt_pk_bf16_f32 v71, v71, v72
	v_add_f32_e32 v95, v93, v77
	v_cvt_pk_bf16_f32 v76, v91, v84
	v_add_f32_e32 v69, v95, v153
	v_add_f32_e32 v68, v94, v152
	v_exp_f32_e32 v95, v96
	v_add_f32_e32 v79, v68, v69
	v_exp_f32_e32 v153, v80
	v_exp_f32_e32 v78, v97
	v_exp_f32_e32 v96, v81
	v_cvt_pk_bf16_f32 v77, v77, v152
	v_add_f32_e32 v97, v153, v95
	v_cvt_pk_bf16_f32 v80, v161, v92
	v_add_f32_e32 v69, v97, v79
	v_add_f32_e32 v68, v96, v78
	v_exp_f32_e32 v97, v98
	v_add_f32_e32 v155, v68, v69
	v_cvt_pk_bf16_f32 v68, v2, v151
	v_add_u32_e32 v2, s74, v1
	v_cvt_pk_bf16_f32 v69, v86, v87
	s_nop 0
	ds_read_b64_tr_b16 v[72:73], v2 offset:32768
	ds_read_b64_tr_b16 v[74:75], v2 offset:33280
	v_exp_f32_e32 v154, v99
	s_waitcnt lgkmcnt(0)
	v_mfma_f32_32x32x16_bf16 v[52:67], v[68:71], v[72:75], v[52:67]
	ds_read_b64_tr_b16 v[84:85], v2 offset:33792
	ds_read_b64_tr_b16 v[86:87], v2 offset:34304
	v_cvt_pk_bf16_f32 v78, v95, v78
	v_cvt_pk_bf16_f32 v79, v97, v154
	v_cvt_pk_bf16_f32 v72, v135, v156
	v_cvt_pk_bf16_f32 v73, v157, v158
	v_cvt_pk_bf16_f32 v74, v160, v88
	v_cvt_pk_bf16_f32 v75, v89, v90
	s_waitcnt lgkmcnt(0)
	v_mfma_f32_32x32x16_bf16 v[52:67], v[76:79], v[84:87], v[52:67]
	ds_read_b64_tr_b16 v[84:85], v2 offset:34816
	ds_read_b64_tr_b16 v[86:87], v2 offset:35328
	v_exp_f32_e32 v95, v82
	v_exp_f32_e32 v98, v83
	ds_read_b64_tr_b16 v[88:89], v2 offset:35840
	ds_read_b64_tr_b16 v[90:91], v2 offset:36352
	v_cvt_pk_bf16_f32 v81, v93, v94
	v_cvt_pk_bf16_f32 v82, v153, v96
	v_cvt_pk_bf16_f32 v83, v95, v98
	s_waitcnt lgkmcnt(2)
	v_mfma_f32_32x32x16_bf16 v[52:67], v[72:75], v[84:87], v[52:67]
	v_add_f32_e32 v99, v95, v97
	s_add_i32 s73, s73, 1
	v_add_u32_e32 v147, 64, v147
	v_add_u32_e32 v150, 64, v150
	s_cmp_eq_u32 s73, 4
	s_mov_b64 s[44:45], 0
	s_waitcnt lgkmcnt(0)
	v_mfma_f32_32x32x16_bf16 v[52:67], v[80:83], v[88:91], v[52:67]
	ds_read_b64_tr_b16 v[192:193], v2 offset:36864
	ds_read_b64_tr_b16 v[194:195], v2 offset:37376
	ds_read_b64_tr_b16 v[196:197], v2 offset:37888
	ds_read_b64_tr_b16 v[198:199], v2 offset:38400
	ds_read_b64_tr_b16 v[200:201], v2 offset:38912
	ds_read_b64_tr_b16 v[202:203], v2 offset:39424
	ds_read_b64_tr_b16 v[204:205], v2 offset:39936
	ds_read_b64_tr_b16 v[206:207], v2 offset:40448
	ds_read_b64_tr_b16 v[208:209], v2 offset:40960
	ds_read_b64_tr_b16 v[210:211], v2 offset:41472
	ds_read_b64_tr_b16 v[212:213], v2 offset:41984
	ds_read_b64_tr_b16 v[214:215], v2 offset:42496
	s_waitcnt lgkmcnt(8)
	v_mfma_f32_32x32x16_bf16 v[36:51], v[68:71], v[192:195], v[36:51]
	v_mfma_f32_32x32x16_bf16 v[36:51], v[76:79], v[196:199], v[36:51]
	ds_read_b64_tr_b16 v[216:217], v2 offset:43008
	ds_read_b64_tr_b16 v[218:219], v2 offset:43520
	ds_read_b64_tr_b16 v[220:221], v2 offset:44032
	ds_read_b64_tr_b16 v[222:223], v2 offset:44544
	s_waitcnt lgkmcnt(8)
	v_mfma_f32_32x32x16_bf16 v[36:51], v[72:75], v[200:203], v[36:51]
	v_mfma_f32_32x32x16_bf16 v[36:51], v[80:83], v[204:207], v[36:51]
	ds_read_b64_tr_b16 v[224:225], v2 offset:45056
	ds_read_b64_tr_b16 v[226:227], v2 offset:45568
	ds_read_b64_tr_b16 v[228:229], v2 offset:46080
	ds_read_b64_tr_b16 v[230:231], v2 offset:46592
	s_waitcnt lgkmcnt(8)
	v_mfma_f32_32x32x16_bf16 v[20:35], v[68:71], v[208:211], v[20:35]
	v_mfma_f32_32x32x16_bf16 v[20:35], v[76:79], v[212:215], v[20:35]
	ds_read_b64_tr_b16 v[232:233], v2 offset:47104
	ds_read_b64_tr_b16 v[234:235], v2 offset:47616
	ds_read_b64_tr_b16 v[236:237], v2 offset:48128
	ds_read_b64_tr_b16 v[238:239], v2 offset:48640
	s_waitcnt lgkmcnt(8)
	v_mfma_f32_32x32x16_bf16 v[20:35], v[72:75], v[216:219], v[20:35]
	v_mfma_f32_32x32x16_bf16 v[20:35], v[80:83], v[220:223], v[20:35]
	s_waitcnt lgkmcnt(4)
	v_mfma_f32_32x32x16_bf16 v[4:19], v[68:71], v[224:227], v[4:19]
	v_mfma_f32_32x32x16_bf16 v[4:19], v[76:79], v[228:231], v[4:19]
	s_waitcnt lgkmcnt(0)
	v_mfma_f32_32x32x16_bf16 v[4:19], v[72:75], v[232:235], v[4:19]
	v_add_f32_e64 v68, v98, v154
	v_add_f32_e64 v69, v99, v155
	v_add_f32_e32 v2, v68, v69
	v_add_f32_e32 v149, v149, v2
	v_mfma_f32_32x32x16_bf16 v[4:19], v[80:83], v[236:239], v[4:19]
	s_cbranch_scc1 .LBB0_951
